# v18 plus unit-loop headers of P3/P5/P11/P12: first fragment LDS reads issued ahead of the next-unit scheduler arithmetic (its VGPR temp renamed)
# speedup vs baseline: 1.0065x; 1.0065x over previous
.LBB0_596:
	ds_read_b128 v[0:3], v217
	ds_read_b128 v[4:7], v217 offset:1024
	ds_read_b128 v[8:11], v217 offset:2048
	ds_read_b128 v[12:15], v217 offset:3072
	ds_read_b128 v[16:19], v218
	ds_read_b128 v[20:23], v218 offset:1024
	ds_read_b128 v[24:27], v218 offset:2048
	ds_read_b128 v[28:31], v218 offset:3072
	ds_read_b128 v[32:35], v219
	ds_read_b128 v[36:39], v219 offset:1024
	ds_read_b128 v[40:43], v219 offset:2048
	ds_read_b128 v[44:47], v219 offset:3072
	ds_read_b128 v[48:51], v219 offset:4096
	ds_read_b128 v[52:55], v219 offset:5120
	ds_read_b128 v[56:59], v219 offset:6144
	ds_read_b128 v[60:63], v219 offset:7168
	s_add_i32 s49, s49, 1
	s_mul_i32 s4, s49, s50
	s_mul_hi_u32 s5, s49, s33
	s_add_i32 s5, s5, s4
	s_mul_i32 s4, s49, s33
	s_add_u32 s26, s4, s87
	s_addc_u32 s27, s5, s51
	v_cmp_gt_i64_e32 vcc, s[26:27], v[192:193]
	v_cmp_lt_i64_e64 s[4:5], s[26:27], v[190:191]
	s_cbranch_vccnz .LBB0_602
	s_ashr_i32 s7, s26, 31
	s_lshr_b32 s7, s7, 29
	s_add_i32 s7, s26, s7
	s_and_b32 s9, s7, -8
	s_sub_i32 s9, s26, s9
	s_cmp_gt_i32 s9, -1
	s_mov_b64 s[22:23], -1
	s_cbranch_scc0 .LBB0_599
	s_lshl_b32 s24, s9, 7
	s_mov_b64 s[22:23], 0

.LBB0_601:
	s_ashr_i32 s7, s7, 3
	s_add_i32 s7, s24, s7
	s_ashr_i32 s9, s7, 31
	s_lshr_b32 s9, s9, 26
	s_add_i32 s9, s7, s9
	s_ashr_i32 s22, s9, 6
	s_lshl_b32 s23, s22, 3
	s_sub_i32 s22, 0x80, s23
	s_min_i32 s24, s22, 8
	s_abs_i32 s22, s24
	v_cvt_f32_u32_e32 v255, s22
	s_sub_i32 s26, 0, s22
	s_andn2_b32 s9, s9, 63
	s_sub_i32 s7, s7, s9
	v_rcp_iflag_f32_e32 v255, v255
	s_abs_i32 s9, s7
	s_xor_b32 s25, s7, s24
	s_ashr_i32 s25, s25, 31
	v_mul_f32_e32 v255, 0x4f7ffffe, v255
	v_cvt_u32_f32_e32 v255, v255
	s_nop 0
	v_readfirstlane_b32 s27, v255
	s_mul_i32 s26, s26, s27
	s_mul_hi_u32 s26, s27, s26
	s_add_i32 s27, s27, s26
	s_mul_hi_u32 s26, s9, s27
	s_mul_i32 s27, s26, s22
	s_sub_i32 s9, s9, s27
	s_add_i32 s28, s26, 1
	s_sub_i32 s27, s9, s22
	s_cmp_ge_u32 s9, s22
	s_cselect_b32 s26, s28, s26
	s_cselect_b32 s9, s27, s9
	s_add_i32 s27, s26, 1
	s_cmp_ge_u32 s9, s22
	s_cselect_b32 s9, s27, s26
	s_xor_b32 s9, s9, s25
	s_sub_i32 s22, s9, s25
	s_mul_i32 s9, s22, s24
	s_sub_i32 s7, s7, s9
	s_add_i32 s24, s23, s7
.LBB0_602:
	s_ashr_i32 s25, s24, 31
	s_lshl_b64 s[26:27], s[24:25], 20
	s_add_u32 s26, s44, s26
	s_addc_u32 s27, s45, s27
	s_and_b64 s[28:29], s[4:5], exec
	s_waitcnt lgkmcnt(0)
	s_cselect_b32 s7, s27, s35
	s_cselect_b32 s9, s26, s34
	s_ashr_i32 s23, s22, 31
	s_lshl_b64 s[28:29], s[22:23], 20
	s_add_u32 s28, s46, s28
	s_addc_u32 s29, s47, s29
	s_and_b64 s[36:37], s[4:5], exec
	s_cselect_b32 s23, s29, s31
	s_cselect_b32 s25, s28, s30
	s_add_u32 s36, s34, 0x100
	s_addc_u32 s37, s35, 0
	s_add_u32 s42, s30, 0x100
	s_addc_u32 s43, s31, 0
	s_add_u32 s38, s34, 0x180
	s_addc_u32 s39, s35, 0
	s_add_u32 s40, s30, 0x180
	s_addc_u32 s41, s31, 0
	s_add_u32 s60, s34, 0x80080
	s_addc_u32 s61, s35, 0
	s_add_i32 m0, s48, 0xc000
	s_nop 0
	global_load_lds_dwordx4 v213, s[60:61]
	s_nop 0
	s_add_i32 m0, s48, 0xe000
	s_nop 0
	global_load_lds_dwordx4 v214, s[60:61]
	s_waitcnt vmcnt(8) lgkmcnt(0)
	s_barrier
	v_mfma_f32_16x16x32_bf16 v[64:67], v[0:3], v[32:35], 0
	v_mfma_f32_16x16x32_bf16 v[68:71], v[8:11], v[32:35], 0
	v_mfma_f32_16x16x32_bf16 v[72:75], v[0:3], v[40:43], 0
	v_mfma_f32_16x16x32_bf16 v[76:79], v[8:11], v[40:43], 0
	v_mfma_f32_16x16x32_bf16 v[80:83], v[0:3], v[48:51], 0
	v_mfma_f32_16x16x32_bf16 v[84:87], v[8:11], v[48:51], 0
	v_mfma_f32_16x16x32_bf16 v[88:91], v[0:3], v[56:59], 0
	v_mfma_f32_16x16x32_bf16 v[64:67], v[4:7], v[36:39], v[64:67]
	v_mfma_f32_16x16x32_bf16 v[68:71], v[12:15], v[36:39], v[68:71]
	v_mfma_f32_16x16x32_bf16 v[72:75], v[4:7], v[44:47], v[72:75]
	v_mfma_f32_16x16x32_bf16 v[76:79], v[12:15], v[44:47], v[76:79]
	v_mfma_f32_16x16x32_bf16 v[80:83], v[4:7], v[52:55], v[80:83]
	v_mfma_f32_16x16x32_bf16 v[84:87], v[12:15], v[52:55], v[84:87]
	v_mfma_f32_16x16x32_bf16 v[96:99], v[4:7], v[60:63], v[88:91]
	v_mfma_f32_16x16x32_bf16 v[88:91], v[8:11], v[56:59], 0
	v_mfma_f32_16x16x32_bf16 v[100:103], v[12:15], v[60:63], v[88:91]
	v_mfma_f32_16x16x32_bf16 v[88:91], v[16:19], v[32:35], 0
	v_mfma_f32_16x16x32_bf16 v[32:35], v[24:27], v[32:35], 0
	v_mfma_f32_16x16x32_bf16 v[104:107], v[20:23], v[36:39], v[88:91]
	v_mfma_f32_16x16x32_bf16 v[32:35], v[28:31], v[36:39], v[32:35]
	v_mfma_f32_16x16x32_bf16 v[36:39], v[16:19], v[40:43], 0
	v_mfma_f32_16x16x32_bf16 v[40:43], v[24:27], v[40:43], 0
	v_mfma_f32_16x16x32_bf16 v[36:39], v[20:23], v[44:47], v[36:39]
	v_mfma_f32_16x16x32_bf16 v[40:43], v[28:31], v[44:47], v[40:43]
	v_mfma_f32_16x16x32_bf16 v[44:47], v[16:19], v[48:51], 0
	v_mfma_f32_16x16x32_bf16 v[48:51], v[24:27], v[48:51], 0
	v_mfma_f32_16x16x32_bf16 v[44:47], v[20:23], v[52:55], v[44:47]
	v_mfma_f32_16x16x32_bf16 v[48:51], v[28:31], v[52:55], v[48:51]
	v_mfma_f32_16x16x32_bf16 v[52:55], v[16:19], v[56:59], 0
	v_mfma_f32_16x16x32_bf16 v[56:59], v[24:27], v[56:59], 0
	v_mfma_f32_16x16x32_bf16 v[52:55], v[20:23], v[60:63], v[52:55]
	v_mfma_f32_16x16x32_bf16 v[56:59], v[28:31], v[60:63], v[56:59]
	s_barrier
	ds_read_b128 v[60:63], v219 offset:16384
	ds_read_b128 v[88:91], v219 offset:17408
	ds_read_b128 v[92:95], v219 offset:18432
	ds_read_b128 v[108:111], v219 offset:19456
	ds_read_b128 v[112:115], v219 offset:20480
	ds_read_b128 v[116:119], v219 offset:21504
	ds_read_b128 v[120:123], v219 offset:22528
	ds_read_b128 v[124:127], v219 offset:23552
	s_add_i32 m0, s48, 0x10000
	s_nop 0
	global_load_lds_dwordx4 v213, s[42:43]
	s_nop 0
	s_add_i32 m0, s48, 0x12000
	s_nop 0
	global_load_lds_dwordx4 v214, s[42:43]
	s_add_u32 s42, s30, 0x80100
	s_addc_u32 s43, s31, 0
	s_add_i32 m0, s48, 0x14000
	s_nop 0
	global_load_lds_dwordx4 v213, s[42:43]
	s_nop 0
	s_add_i32 m0, s48, 0x16000
	s_nop 0
	global_load_lds_dwordx4 v214, s[42:43]
	s_nop 0
	s_add_i32 m0, s48, 0
	s_nop 0
	global_load_lds_dwordx4 v213, s[36:37]
	s_nop 0
	s_add_i32 m0, s48, 0x2000
	s_nop 0
	global_load_lds_dwordx4 v214, s[36:37]
	s_waitcnt vmcnt(8) lgkmcnt(0)
	s_barrier
	v_mfma_f32_16x16x32_bf16 v[128:131], v[0:3], v[60:63], 0
	v_mfma_f32_16x16x32_bf16 v[132:135], v[4:7], v[88:91], v[128:131]
	v_mfma_f32_16x16x32_bf16 v[128:131], v[8:11], v[60:63], 0
	v_mfma_f32_16x16x32_bf16 v[140:143], v[12:15], v[88:91], v[128:131]
	v_mfma_f32_16x16x32_bf16 v[128:131], v[0:3], v[92:95], 0
	v_mfma_f32_16x16x32_bf16 v[148:151], v[4:7], v[108:111], v[128:131]
	v_mfma_f32_16x16x32_bf16 v[128:131], v[8:11], v[92:95], 0
	v_mfma_f32_16x16x32_bf16 v[156:159], v[12:15], v[108:111], v[128:131]
	v_mfma_f32_16x16x32_bf16 v[128:131], v[0:3], v[112:115], 0
	v_mfma_f32_16x16x32_bf16 v[0:3], v[0:3], v[120:123], 0
	v_mfma_f32_16x16x32_bf16 v[160:163], v[4:7], v[116:119], v[128:131]
	v_mfma_f32_16x16x32_bf16 v[0:3], v[4:7], v[124:127], v[0:3]
	v_mfma_f32_16x16x32_bf16 v[4:7], v[8:11], v[120:123], 0
	v_mfma_f32_16x16x32_bf16 v[128:131], v[8:11], v[112:115], 0
	v_mfma_f32_16x16x32_bf16 v[4:7], v[12:15], v[124:127], v[4:7]
	v_mfma_f32_16x16x32_bf16 v[164:167], v[12:15], v[116:119], v[128:131]
	v_mfma_f32_16x16x32_bf16 v[8:11], v[16:19], v[60:63], 0
	v_mfma_f32_16x16x32_bf16 v[168:171], v[20:23], v[88:91], v[8:11]
	v_mfma_f32_16x16x32_bf16 v[8:11], v[24:27], v[60:63], 0
	v_mfma_f32_16x16x32_bf16 v[172:175], v[28:31], v[88:91], v[8:11]
	v_mfma_f32_16x16x32_bf16 v[8:11], v[16:19], v[92:95], 0
	v_mfma_f32_16x16x32_bf16 v[176:179], v[20:23], v[108:111], v[8:11]
	v_mfma_f32_16x16x32_bf16 v[8:11], v[24:27], v[92:95], 0
	v_mfma_f32_16x16x32_bf16 v[108:111], v[28:31], v[108:111], v[8:11]
	v_mfma_f32_16x16x32_bf16 v[8:11], v[16:19], v[112:115], 0
	v_mfma_f32_16x16x32_bf16 v[180:183], v[20:23], v[116:119], v[8:11]
	v_mfma_f32_16x16x32_bf16 v[8:11], v[24:27], v[112:115], 0
	v_mfma_f32_16x16x32_bf16 v[116:119], v[28:31], v[116:119], v[8:11]
	v_mfma_f32_16x16x32_bf16 v[8:11], v[16:19], v[120:123], 0
	v_mfma_f32_16x16x32_bf16 v[184:187], v[20:23], v[124:127], v[8:11]
	v_mfma_f32_16x16x32_bf16 v[8:11], v[24:27], v[120:123], 0
	v_mfma_f32_16x16x32_bf16 v[124:127], v[28:31], v[124:127], v[8:11]
	s_barrier
	s_nop 4
	ds_read_b128 v[8:11], v220
	ds_read_b128 v[12:15], v220 offset:1024
	ds_read_b128 v[16:19], v220 offset:2048
	ds_read_b128 v[20:23], v220 offset:3072
	ds_read_b128 v[194:197], v221
	ds_read_b128 v[198:201], v221 offset:1024
	ds_read_b128 v[202:205], v221 offset:2048
	ds_read_b128 v[206:209], v221 offset:3072
	ds_read_b128 v[24:27], v219 offset:32768
	ds_read_b128 v[28:31], v219 offset:33792
	ds_read_b128 v[60:63], v219 offset:34816
	ds_read_b128 v[224:227], v219 offset:35840
	ds_read_b128 v[228:231], v219 offset:36864
	ds_read_b128 v[232:235], v219 offset:37888
	ds_read_b128 v[236:239], v219 offset:38912
	ds_read_b128 v[240:243], v219 offset:39936
	s_add_u32 s34, s34, 0x80100
	s_addc_u32 s35, s35, 0
	s_add_i32 m0, s48, 0x4000
	s_nop 0
	global_load_lds_dwordx4 v213, s[34:35]
	s_nop 0
	s_add_i32 m0, s48, 0x6000
	s_nop 0
	global_load_lds_dwordx4 v214, s[34:35]
	s_waitcnt vmcnt(8) lgkmcnt(0)
	s_barrier
	v_mfma_f32_16x16x32_bf16 v[64:67], v[8:11], v[24:27], v[64:67]
	v_mfma_f32_16x16x32_bf16 v[152:155], v[12:15], v[28:31], v[64:67]
	v_mfma_f32_16x16x32_bf16 v[64:67], v[16:19], v[24:27], v[68:71]
	v_mfma_f32_16x16x32_bf16 v[144:147], v[20:23], v[28:31], v[64:67]
	v_mfma_f32_16x16x32_bf16 v[64:67], v[8:11], v[60:63], v[72:75]
	v_mfma_f32_16x16x32_bf16 v[120:123], v[12:15], v[224:227], v[64:67]
	v_mfma_f32_16x16x32_bf16 v[64:67], v[16:19], v[60:63], v[76:79]
	v_mfma_f32_16x16x32_bf16 v[112:115], v[20:23], v[224:227], v[64:67]
	v_mfma_f32_16x16x32_bf16 v[64:67], v[8:11], v[228:231], v[80:83]
	v_mfma_f32_16x16x32_bf16 v[92:95], v[12:15], v[232:235], v[64:67]
	v_mfma_f32_16x16x32_bf16 v[64:67], v[16:19], v[228:231], v[84:87]
	v_mfma_f32_16x16x32_bf16 v[88:91], v[20:23], v[232:235], v[64:67]
	v_mfma_f32_16x16x32_bf16 v[64:67], v[8:11], v[236:239], v[96:99]
	v_mfma_f32_16x16x32_bf16 v[76:79], v[12:15], v[240:243], v[64:67]
	v_mfma_f32_16x16x32_bf16 v[64:67], v[16:19], v[236:239], v[100:103]
	v_mfma_f32_16x16x32_bf16 v[72:75], v[20:23], v[240:243], v[64:67]
	v_mfma_f32_16x16x32_bf16 v[64:67], v[194:197], v[24:27], v[104:107]
	v_mfma_f32_16x16x32_bf16 v[24:27], v[202:205], v[24:27], v[32:35]
	v_mfma_f32_16x16x32_bf16 v[128:131], v[206:209], v[28:31], v[24:27]
	v_mfma_f32_16x16x32_bf16 v[24:27], v[194:197], v[60:63], v[36:39]
	v_mfma_f32_16x16x32_bf16 v[104:107], v[198:201], v[224:227], v[24:27]
	v_mfma_f32_16x16x32_bf16 v[24:27], v[202:205], v[60:63], v[40:43]
	v_mfma_f32_16x16x32_bf16 v[96:99], v[206:209], v[224:227], v[24:27]
	v_mfma_f32_16x16x32_bf16 v[24:27], v[194:197], v[228:231], v[44:47]
	v_mfma_f32_16x16x32_bf16 v[84:87], v[198:201], v[232:235], v[24:27]
	v_mfma_f32_16x16x32_bf16 v[24:27], v[202:205], v[228:231], v[48:51]
	v_mfma_f32_16x16x32_bf16 v[80:83], v[206:209], v[232:235], v[24:27]
	v_mfma_f32_16x16x32_bf16 v[24:27], v[194:197], v[236:239], v[52:55]
	v_mfma_f32_16x16x32_bf16 v[68:71], v[198:201], v[240:243], v[24:27]
	v_mfma_f32_16x16x32_bf16 v[24:27], v[202:205], v[236:239], v[56:59]
	v_mfma_f32_16x16x32_bf16 v[136:139], v[198:201], v[28:31], v[64:67]
	v_mfma_f32_16x16x32_bf16 v[64:67], v[206:209], v[240:243], v[24:27]
	s_barrier
	ds_read_b128 v[32:35], v219 offset:49152
	ds_read_b128 v[36:39], v219 offset:50176
	ds_read_b128 v[100:103], v219 offset:51200
	ds_read_b128 v[224:227], v219 offset:52224
	ds_read_b128 v[228:231], v219 offset:53248
	ds_read_b128 v[232:235], v219 offset:54272
	ds_read_b128 v[236:239], v219 offset:55296
	ds_read_b128 v[240:243], v219 offset:56320
	s_add_i32 m0, s48, 0x18000
	s_nop 0
	global_load_lds_dwordx4 v213, s[40:41]
	s_nop 0
	s_add_i32 m0, s48, 0x1a000
	s_nop 0
	global_load_lds_dwordx4 v214, s[40:41]
	s_add_u32 s34, s30, 0x80180
	s_addc_u32 s35, s31, 0
	s_add_i32 m0, s48, 0x1c000
	s_nop 0
	global_load_lds_dwordx4 v213, s[34:35]
	s_nop 0
	s_add_i32 m0, s48, 0x1e000
	s_nop 0
	global_load_lds_dwordx4 v214, s[34:35]
	s_nop 0
	s_add_i32 m0, s48, 0x8000
	s_nop 0
	global_load_lds_dwordx4 v213, s[38:39]
	s_nop 0
	s_add_i32 m0, s48, 0xa000
	s_nop 0
	global_load_lds_dwordx4 v214, s[38:39]
	s_waitcnt vmcnt(8) lgkmcnt(0)
	s_barrier
	v_mfma_f32_16x16x32_bf16 v[24:27], v[8:11], v[32:35], v[132:135]
	v_mfma_f32_16x16x32_bf16 v[60:63], v[12:15], v[36:39], v[24:27]
	v_mfma_f32_16x16x32_bf16 v[24:27], v[16:19], v[32:35], v[140:143]
	v_mfma_f32_16x16x32_bf16 v[56:59], v[20:23], v[36:39], v[24:27]
	v_mfma_f32_16x16x32_bf16 v[24:27], v[8:11], v[100:103], v[148:151]
	v_mfma_f32_16x16x32_bf16 v[44:47], v[12:15], v[224:227], v[24:27]
	v_mfma_f32_16x16x32_bf16 v[24:27], v[16:19], v[100:103], v[156:159]
	v_mfma_f32_16x16x32_bf16 v[40:43], v[20:23], v[224:227], v[24:27]
	v_mfma_f32_16x16x32_bf16 v[24:27], v[8:11], v[228:231], v[160:163]
	v_mfma_f32_16x16x32_bf16 v[0:3], v[8:11], v[236:239], v[0:3]
	v_mfma_f32_16x16x32_bf16 v[28:31], v[12:15], v[232:235], v[24:27]
	v_mfma_f32_16x16x32_bf16 v[24:27], v[16:19], v[228:231], v[164:167]
	v_mfma_f32_16x16x32_bf16 v[12:15], v[12:15], v[240:243], v[0:3]
	v_mfma_f32_16x16x32_bf16 v[0:3], v[16:19], v[236:239], v[4:7]
	v_mfma_f32_16x16x32_bf16 v[24:27], v[20:23], v[232:235], v[24:27]
	v_mfma_f32_16x16x32_bf16 v[8:11], v[20:23], v[240:243], v[0:3]
	v_mfma_f32_16x16x32_bf16 v[0:3], v[194:197], v[32:35], v[168:171]
	v_mfma_f32_16x16x32_bf16 v[52:55], v[198:201], v[36:39], v[0:3]
	v_mfma_f32_16x16x32_bf16 v[0:3], v[202:205], v[32:35], v[172:175]
	v_mfma_f32_16x16x32_bf16 v[48:51], v[206:209], v[36:39], v[0:3]
	v_mfma_f32_16x16x32_bf16 v[0:3], v[194:197], v[100:103], v[176:179]
	v_mfma_f32_16x16x32_bf16 v[36:39], v[198:201], v[224:227], v[0:3]
	v_mfma_f32_16x16x32_bf16 v[0:3], v[202:205], v[100:103], v[108:111]
	v_mfma_f32_16x16x32_bf16 v[32:35], v[206:209], v[224:227], v[0:3]
	v_mfma_f32_16x16x32_bf16 v[0:3], v[194:197], v[228:231], v[180:183]
	v_mfma_f32_16x16x32_bf16 v[20:23], v[198:201], v[232:235], v[0:3]
	v_mfma_f32_16x16x32_bf16 v[0:3], v[202:205], v[228:231], v[116:119]
	v_mfma_f32_16x16x32_bf16 v[16:19], v[206:209], v[232:235], v[0:3]
	v_mfma_f32_16x16x32_bf16 v[0:3], v[194:197], v[236:239], v[184:187]
	v_mfma_f32_16x16x32_bf16 v[4:7], v[198:201], v[240:243], v[0:3]
	v_mfma_f32_16x16x32_bf16 v[0:3], v[202:205], v[236:239], v[124:127]
	v_mfma_f32_16x16x32_bf16 v[0:3], v[206:209], v[240:243], v[0:3]
	s_barrier
	s_add_u32 s59, s30, 0x200
	s_addc_u32 s60, s31, 0
	s_mov_b32 s61, 0

.LBB0_827:
	ds_read_b128 v[0:3], v181
	ds_read_b128 v[4:7], v181 offset:1024
	ds_read_b128 v[8:11], v181 offset:2048
	ds_read_b128 v[12:15], v181 offset:3072
	ds_read_b128 v[16:19], v182
	ds_read_b128 v[20:23], v182 offset:1024
	ds_read_b128 v[24:27], v182 offset:2048
	ds_read_b128 v[28:31], v182 offset:3072
	ds_read_b128 v[32:35], v183
	ds_read_b128 v[36:39], v183 offset:1024
	ds_read_b128 v[40:43], v183 offset:2048
	ds_read_b128 v[44:47], v183 offset:3072
	ds_read_b128 v[48:51], v183 offset:4096
	ds_read_b128 v[52:55], v183 offset:5120
	ds_read_b128 v[56:59], v183 offset:6144
	ds_read_b128 v[60:63], v183 offset:7168
	s_add_i32 s37, s37, 1
	s_mul_i32 s4, s37, s38
	s_mul_hi_u32 s5, s37, s33
	s_add_i32 s5, s5, s4
	s_mul_i32 s4, s37, s33
	s_add_u32 s4, s4, s87
	s_addc_u32 s5, s5, s39
	v_cmp_gt_i64_e32 vcc, s[4:5], v[154:155]
	v_cmp_lt_i64_e64 s[6:7], s[4:5], v[152:153]
	s_cbranch_vccnz .LBB0_833
	s_ashr_i32 s5, s4, 31
	s_lshr_b32 s5, s5, 29
	s_add_i32 s18, s4, s5
	s_and_b32 s5, s18, -8
	s_sub_i32 s19, s4, s5
	s_cmp_gt_i32 s19, -1
	s_mov_b64 s[4:5], -1
	s_cbranch_scc0 .LBB0_830
	s_lshl_b32 s20, s19, 7
	s_mov_b64 s[4:5], 0

.LBB0_832:
	s_ashr_i32 s4, s18, 3
	s_add_i32 s4, s20, s4
	s_ashr_i32 s5, s4, 31
	s_lshr_b32 s5, s5, 26
	s_add_i32 s5, s4, s5
	s_ashr_i32 s18, s5, 6
	s_lshl_b32 s18, s18, 3
	s_sub_i32 s19, 0x80, s18
	s_min_i32 s19, s19, 8
	s_abs_i32 s20, s19
	v_cvt_f32_u32_e32 v255, s20
	s_sub_i32 s26, 0, s20
	s_andn2_b32 s5, s5, 63
	s_sub_i32 s4, s4, s5
	v_rcp_iflag_f32_e32 v255, v255
	s_abs_i32 s5, s4
	s_xor_b32 s21, s4, s19
	s_ashr_i32 s21, s21, 31
	v_mul_f32_e32 v255, 0x4f7ffffe, v255
	v_cvt_u32_f32_e32 v255, v255
	s_nop 0
	v_readfirstlane_b32 s27, v255
	s_mul_i32 s26, s26, s27
	s_mul_hi_u32 s26, s27, s26
	s_add_i32 s27, s27, s26
	s_mul_hi_u32 s26, s5, s27
	s_mul_i32 s27, s26, s20
	s_sub_i32 s5, s5, s27
	s_add_i32 s28, s26, 1
	s_sub_i32 s27, s5, s20
	s_cmp_ge_u32 s5, s20
	s_cselect_b32 s26, s28, s26
	s_cselect_b32 s5, s27, s5
	s_add_i32 s27, s26, 1
	s_cmp_ge_u32 s5, s20
	s_cselect_b32 s5, s27, s26
	s_xor_b32 s5, s5, s21
	s_sub_i32 s47, s5, s21
	s_mul_i32 s5, s47, s19
	s_sub_i32 s4, s4, s5
	s_add_i32 s48, s18, s4
.LBB0_833:
	s_nop 0
	v_cndmask_b32_e64 v255, 0, 1, s[6:7]
	v_cmp_ne_u32_e64 s[4:5], 1, v255
	s_andn2_b64 vcc, exec, s[6:7]
	s_mov_b64 s[18:19], s[22:23]
	s_cbranch_vccnz .LBB0_835
	s_mul_i32 s7, s48, 0x2c0000
	s_mul_hi_i32 s6, s48, 0x2c0000
	s_add_u32 s18, s30, s7
	s_addc_u32 s19, s31, s6

.LBB0_837:
	s_waitcnt lgkmcnt(0)
	s_add_u32 s28, s22, 0x100
	s_addc_u32 s29, s23, 0
	s_add_u32 s52, s24, 0x100
	s_addc_u32 s53, s25, 0
	s_add_u32 s6, s22, 0x180
	s_addc_u32 s7, s23, 0
	s_add_u32 s26, s24, 0x180
	s_addc_u32 s27, s25, 0
	s_add_u32 s54, s22, 0x160080
	s_addc_u32 s55, s23, 0
	s_add_i32 m0, s36, 0xc000
	s_nop 0
	global_load_lds_dwordx4 v175, s[54:55]
	s_nop 0
	s_add_i32 m0, s36, 0xe000
	s_nop 0
	global_load_lds_dwordx4 v177, s[54:55]
	s_waitcnt vmcnt(8) lgkmcnt(0)
	s_barrier
	v_mfma_f32_16x16x32_bf16 v[88:91], v[0:3], v[56:59], 0
	v_mfma_f32_16x16x32_bf16 v[64:67], v[0:3], v[32:35], 0
	v_mfma_f32_16x16x32_bf16 v[68:71], v[8:11], v[32:35], 0
	v_mfma_f32_16x16x32_bf16 v[72:75], v[0:3], v[40:43], 0
	v_mfma_f32_16x16x32_bf16 v[76:79], v[8:11], v[40:43], 0
	v_mfma_f32_16x16x32_bf16 v[80:83], v[0:3], v[48:51], 0
	v_mfma_f32_16x16x32_bf16 v[84:87], v[8:11], v[48:51], 0
	v_mfma_f32_16x16x32_bf16 v[96:99], v[4:7], v[60:63], v[88:91]
	v_mfma_f32_16x16x32_bf16 v[88:91], v[8:11], v[56:59], 0
	v_mfma_f32_16x16x32_bf16 v[64:67], v[4:7], v[36:39], v[64:67]
	v_mfma_f32_16x16x32_bf16 v[68:71], v[12:15], v[36:39], v[68:71]
	v_mfma_f32_16x16x32_bf16 v[72:75], v[4:7], v[44:47], v[72:75]
	v_mfma_f32_16x16x32_bf16 v[76:79], v[12:15], v[44:47], v[76:79]
	v_mfma_f32_16x16x32_bf16 v[80:83], v[4:7], v[52:55], v[80:83]
	v_mfma_f32_16x16x32_bf16 v[84:87], v[12:15], v[52:55], v[84:87]
	v_mfma_f32_16x16x32_bf16 v[100:103], v[12:15], v[60:63], v[88:91]
	v_mfma_f32_16x16x32_bf16 v[88:91], v[16:19], v[32:35], 0
	v_mfma_f32_16x16x32_bf16 v[32:35], v[24:27], v[32:35], 0
	v_mfma_f32_16x16x32_bf16 v[112:115], v[20:23], v[36:39], v[88:91]
	v_mfma_f32_16x16x32_bf16 v[32:35], v[28:31], v[36:39], v[32:35]
	v_mfma_f32_16x16x32_bf16 v[36:39], v[16:19], v[40:43], 0
	v_mfma_f32_16x16x32_bf16 v[40:43], v[24:27], v[40:43], 0
	v_mfma_f32_16x16x32_bf16 v[36:39], v[20:23], v[44:47], v[36:39]
	v_mfma_f32_16x16x32_bf16 v[40:43], v[28:31], v[44:47], v[40:43]
	v_mfma_f32_16x16x32_bf16 v[44:47], v[16:19], v[48:51], 0
	v_mfma_f32_16x16x32_bf16 v[48:51], v[24:27], v[48:51], 0
	v_mfma_f32_16x16x32_bf16 v[44:47], v[20:23], v[52:55], v[44:47]
	v_mfma_f32_16x16x32_bf16 v[48:51], v[28:31], v[52:55], v[48:51]
	v_mfma_f32_16x16x32_bf16 v[52:55], v[16:19], v[56:59], 0
	v_mfma_f32_16x16x32_bf16 v[56:59], v[24:27], v[56:59], 0
	v_mfma_f32_16x16x32_bf16 v[52:55], v[20:23], v[60:63], v[52:55]
	v_mfma_f32_16x16x32_bf16 v[56:59], v[28:31], v[60:63], v[56:59]
	s_barrier
	ds_read_b128 v[60:63], v183 offset:16384
	ds_read_b128 v[88:91], v183 offset:17408
	ds_read_b128 v[92:95], v183 offset:18432
	ds_read_b128 v[104:107], v183 offset:19456
	ds_read_b128 v[108:111], v183 offset:20480
	ds_read_b128 v[116:119], v183 offset:21504
	ds_read_b128 v[120:123], v183 offset:22528
	ds_read_b128 v[124:127], v183 offset:23552
	s_add_i32 m0, s36, 0x10000
	s_nop 0
	global_load_lds_dwordx4 v176, s[52:53]
	s_nop 0
	s_add_i32 m0, s36, 0x12000
	s_nop 0
	global_load_lds_dwordx4 v178, s[52:53]
	s_add_u32 s52, s24, 0x160100
	s_addc_u32 s53, s25, 0
	s_add_i32 m0, s36, 0x14000
	s_nop 0
	global_load_lds_dwordx4 v176, s[52:53]
	s_nop 0
	s_add_i32 m0, s36, 0x16000
	s_nop 0
	global_load_lds_dwordx4 v178, s[52:53]
	s_nop 0
	s_add_i32 m0, s36, 0
	s_nop 0
	global_load_lds_dwordx4 v175, s[28:29]
	s_nop 0
	s_add_i32 m0, s36, 0x2000
	s_nop 0
	global_load_lds_dwordx4 v177, s[28:29]
	s_waitcnt vmcnt(8) lgkmcnt(0)
	s_barrier
	v_mfma_f32_16x16x32_bf16 v[128:131], v[0:3], v[60:63], 0
	v_mfma_f32_16x16x32_bf16 v[136:139], v[4:7], v[88:91], v[128:131]
	v_mfma_f32_16x16x32_bf16 v[128:131], v[8:11], v[60:63], 0
	v_mfma_f32_16x16x32_bf16 v[140:143], v[12:15], v[88:91], v[128:131]
	v_mfma_f32_16x16x32_bf16 v[128:131], v[0:3], v[92:95], 0
	v_mfma_f32_16x16x32_bf16 v[144:147], v[4:7], v[104:107], v[128:131]
	v_mfma_f32_16x16x32_bf16 v[128:131], v[8:11], v[92:95], 0
	v_mfma_f32_16x16x32_bf16 v[148:151], v[12:15], v[104:107], v[128:131]
	v_mfma_f32_16x16x32_bf16 v[128:131], v[0:3], v[108:111], 0
	v_mfma_f32_16x16x32_bf16 v[0:3], v[0:3], v[120:123], 0
	v_mfma_f32_16x16x32_bf16 v[156:159], v[4:7], v[116:119], v[128:131]
	v_mfma_f32_16x16x32_bf16 v[0:3], v[4:7], v[124:127], v[0:3]
	v_mfma_f32_16x16x32_bf16 v[4:7], v[8:11], v[120:123], 0
	v_mfma_f32_16x16x32_bf16 v[128:131], v[8:11], v[108:111], 0
	v_mfma_f32_16x16x32_bf16 v[4:7], v[12:15], v[124:127], v[4:7]
	v_mfma_f32_16x16x32_bf16 v[160:163], v[12:15], v[116:119], v[128:131]
	v_mfma_f32_16x16x32_bf16 v[8:11], v[16:19], v[60:63], 0
	v_mfma_f32_16x16x32_bf16 v[164:167], v[20:23], v[88:91], v[8:11]
	v_mfma_f32_16x16x32_bf16 v[8:11], v[24:27], v[60:63], 0
	v_mfma_f32_16x16x32_bf16 v[168:171], v[28:31], v[88:91], v[8:11]
	v_mfma_f32_16x16x32_bf16 v[8:11], v[16:19], v[92:95], 0
	v_mfma_f32_16x16x32_bf16 v[188:191], v[20:23], v[104:107], v[8:11]
	v_mfma_f32_16x16x32_bf16 v[8:11], v[24:27], v[92:95], 0
	v_mfma_f32_16x16x32_bf16 v[192:195], v[28:31], v[104:107], v[8:11]
	v_mfma_f32_16x16x32_bf16 v[8:11], v[16:19], v[108:111], 0
	v_mfma_f32_16x16x32_bf16 v[196:199], v[20:23], v[116:119], v[8:11]
	v_mfma_f32_16x16x32_bf16 v[8:11], v[24:27], v[108:111], 0
	v_mfma_f32_16x16x32_bf16 v[116:119], v[28:31], v[116:119], v[8:11]
	v_mfma_f32_16x16x32_bf16 v[8:11], v[16:19], v[120:123], 0
	v_mfma_f32_16x16x32_bf16 v[200:203], v[20:23], v[124:127], v[8:11]
	v_mfma_f32_16x16x32_bf16 v[8:11], v[24:27], v[120:123], 0
	v_mfma_f32_16x16x32_bf16 v[204:207], v[28:31], v[124:127], v[8:11]
	s_barrier
	s_nop 4
	ds_read_b128 v[8:11], v184
	ds_read_b128 v[12:15], v184 offset:1024
	ds_read_b128 v[16:19], v184 offset:2048
	ds_read_b128 v[20:23], v184 offset:3072
	ds_read_b128 v[208:211], v185
	ds_read_b128 v[212:215], v185 offset:1024
	ds_read_b128 v[216:219], v185 offset:2048
	ds_read_b128 v[220:223], v185 offset:3072
	ds_read_b128 v[24:27], v183 offset:32768
	ds_read_b128 v[28:31], v183 offset:33792
	ds_read_b128 v[60:63], v183 offset:34816
	ds_read_b128 v[224:227], v183 offset:35840
	ds_read_b128 v[228:231], v183 offset:36864
	ds_read_b128 v[232:235], v183 offset:37888
	ds_read_b128 v[236:239], v183 offset:38912
	ds_read_b128 v[240:243], v183 offset:39936
	s_add_u32 s28, s22, 0x160100
	s_addc_u32 s29, s23, 0
	s_add_i32 m0, s36, 0x4000
	s_nop 0
	global_load_lds_dwordx4 v175, s[28:29]
	s_nop 0
	s_add_i32 m0, s36, 0x6000
	s_nop 0
	global_load_lds_dwordx4 v177, s[28:29]
	s_waitcnt vmcnt(8) lgkmcnt(0)
	s_barrier
	v_mfma_f32_16x16x32_bf16 v[64:67], v[8:11], v[24:27], v[64:67]
	v_mfma_f32_16x16x32_bf16 v[132:135], v[12:15], v[28:31], v[64:67]
	v_mfma_f32_16x16x32_bf16 v[64:67], v[16:19], v[24:27], v[68:71]
	v_mfma_f32_16x16x32_bf16 v[128:131], v[20:23], v[28:31], v[64:67]
	v_mfma_f32_16x16x32_bf16 v[64:67], v[8:11], v[60:63], v[72:75]
	v_mfma_f32_16x16x32_bf16 v[108:111], v[12:15], v[224:227], v[64:67]
	v_mfma_f32_16x16x32_bf16 v[64:67], v[16:19], v[60:63], v[76:79]
	v_mfma_f32_16x16x32_bf16 v[104:107], v[20:23], v[224:227], v[64:67]
	v_mfma_f32_16x16x32_bf16 v[64:67], v[8:11], v[228:231], v[80:83]
	v_mfma_f32_16x16x32_bf16 v[92:95], v[12:15], v[232:235], v[64:67]
	v_mfma_f32_16x16x32_bf16 v[64:67], v[16:19], v[228:231], v[84:87]
	v_mfma_f32_16x16x32_bf16 v[88:91], v[20:23], v[232:235], v[64:67]
	v_mfma_f32_16x16x32_bf16 v[64:67], v[8:11], v[236:239], v[96:99]
	v_mfma_f32_16x16x32_bf16 v[76:79], v[12:15], v[240:243], v[64:67]
	v_mfma_f32_16x16x32_bf16 v[64:67], v[16:19], v[236:239], v[100:103]
	v_mfma_f32_16x16x32_bf16 v[72:75], v[20:23], v[240:243], v[64:67]
	v_mfma_f32_16x16x32_bf16 v[64:67], v[208:211], v[24:27], v[112:115]
	v_mfma_f32_16x16x32_bf16 v[24:27], v[216:219], v[24:27], v[32:35]
	v_mfma_f32_16x16x32_bf16 v[120:123], v[220:223], v[28:31], v[24:27]
	v_mfma_f32_16x16x32_bf16 v[24:27], v[208:211], v[60:63], v[36:39]
	v_mfma_f32_16x16x32_bf16 v[100:103], v[212:215], v[224:227], v[24:27]
	v_mfma_f32_16x16x32_bf16 v[24:27], v[216:219], v[60:63], v[40:43]
	v_mfma_f32_16x16x32_bf16 v[96:99], v[220:223], v[224:227], v[24:27]
	v_mfma_f32_16x16x32_bf16 v[24:27], v[208:211], v[228:231], v[44:47]
	v_mfma_f32_16x16x32_bf16 v[84:87], v[212:215], v[232:235], v[24:27]
	v_mfma_f32_16x16x32_bf16 v[24:27], v[216:219], v[228:231], v[48:51]
	v_mfma_f32_16x16x32_bf16 v[80:83], v[220:223], v[232:235], v[24:27]
	v_mfma_f32_16x16x32_bf16 v[24:27], v[208:211], v[236:239], v[52:55]
	v_mfma_f32_16x16x32_bf16 v[68:71], v[212:215], v[240:243], v[24:27]
	v_mfma_f32_16x16x32_bf16 v[24:27], v[216:219], v[236:239], v[56:59]
	v_mfma_f32_16x16x32_bf16 v[124:127], v[212:215], v[28:31], v[64:67]
	v_mfma_f32_16x16x32_bf16 v[64:67], v[220:223], v[240:243], v[24:27]
	s_barrier
	ds_read_b128 v[32:35], v183 offset:49152
	ds_read_b128 v[36:39], v183 offset:50176
	ds_read_b128 v[112:115], v183 offset:51200
	ds_read_b128 v[224:227], v183 offset:52224
	ds_read_b128 v[228:231], v183 offset:53248
	ds_read_b128 v[232:235], v183 offset:54272
	ds_read_b128 v[236:239], v183 offset:55296
	ds_read_b128 v[240:243], v183 offset:56320
	s_add_i32 m0, s36, 0x18000
	s_nop 0
	global_load_lds_dwordx4 v176, s[26:27]
	s_nop 0
	s_add_i32 m0, s36, 0x1a000
	s_nop 0
	global_load_lds_dwordx4 v178, s[26:27]
	s_add_u32 s26, s24, 0x160180
	s_addc_u32 s27, s25, 0
	s_add_i32 m0, s36, 0x1c000
	s_nop 0
	global_load_lds_dwordx4 v176, s[26:27]
	s_nop 0
	s_add_i32 m0, s36, 0x1e000
	s_nop 0
	global_load_lds_dwordx4 v178, s[26:27]
	s_nop 0
	s_add_i32 m0, s36, 0x8000
	s_nop 0
	global_load_lds_dwordx4 v175, s[6:7]
	s_nop 0
	s_add_i32 m0, s36, 0xa000
	s_nop 0
	global_load_lds_dwordx4 v177, s[6:7]
	s_waitcnt vmcnt(8) lgkmcnt(0)
	s_barrier
	v_mfma_f32_16x16x32_bf16 v[24:27], v[8:11], v[32:35], v[136:139]
	v_mfma_f32_16x16x32_bf16 v[60:63], v[12:15], v[36:39], v[24:27]
	v_mfma_f32_16x16x32_bf16 v[24:27], v[16:19], v[32:35], v[140:143]
	v_mfma_f32_16x16x32_bf16 v[56:59], v[20:23], v[36:39], v[24:27]
	v_mfma_f32_16x16x32_bf16 v[24:27], v[8:11], v[112:115], v[144:147]
	v_mfma_f32_16x16x32_bf16 v[44:47], v[12:15], v[224:227], v[24:27]
	v_mfma_f32_16x16x32_bf16 v[24:27], v[16:19], v[112:115], v[148:151]
	v_mfma_f32_16x16x32_bf16 v[40:43], v[20:23], v[224:227], v[24:27]
	v_mfma_f32_16x16x32_bf16 v[24:27], v[8:11], v[228:231], v[156:159]
	v_mfma_f32_16x16x32_bf16 v[0:3], v[8:11], v[236:239], v[0:3]
	v_mfma_f32_16x16x32_bf16 v[28:31], v[12:15], v[232:235], v[24:27]
	v_mfma_f32_16x16x32_bf16 v[24:27], v[16:19], v[228:231], v[160:163]
	v_mfma_f32_16x16x32_bf16 v[12:15], v[12:15], v[240:243], v[0:3]
	v_mfma_f32_16x16x32_bf16 v[0:3], v[16:19], v[236:239], v[4:7]
	v_mfma_f32_16x16x32_bf16 v[24:27], v[20:23], v[232:235], v[24:27]
	v_mfma_f32_16x16x32_bf16 v[8:11], v[20:23], v[240:243], v[0:3]
	v_mfma_f32_16x16x32_bf16 v[0:3], v[208:211], v[32:35], v[164:167]
	v_mfma_f32_16x16x32_bf16 v[52:55], v[212:215], v[36:39], v[0:3]
	v_mfma_f32_16x16x32_bf16 v[0:3], v[216:219], v[32:35], v[168:171]
	v_mfma_f32_16x16x32_bf16 v[48:51], v[220:223], v[36:39], v[0:3]
	v_mfma_f32_16x16x32_bf16 v[0:3], v[208:211], v[112:115], v[188:191]
	v_mfma_f32_16x16x32_bf16 v[36:39], v[212:215], v[224:227], v[0:3]
	v_mfma_f32_16x16x32_bf16 v[0:3], v[216:219], v[112:115], v[192:195]
	v_mfma_f32_16x16x32_bf16 v[32:35], v[220:223], v[224:227], v[0:3]
	v_mfma_f32_16x16x32_bf16 v[0:3], v[208:211], v[228:231], v[196:199]
	v_mfma_f32_16x16x32_bf16 v[20:23], v[212:215], v[232:235], v[0:3]
	v_mfma_f32_16x16x32_bf16 v[0:3], v[216:219], v[228:231], v[116:119]
	v_mfma_f32_16x16x32_bf16 v[16:19], v[220:223], v[232:235], v[0:3]
	v_mfma_f32_16x16x32_bf16 v[0:3], v[208:211], v[236:239], v[200:203]
	v_mfma_f32_16x16x32_bf16 v[4:7], v[212:215], v[240:243], v[0:3]
	v_mfma_f32_16x16x32_bf16 v[0:3], v[216:219], v[236:239], v[204:207]
	v_mfma_f32_16x16x32_bf16 v[0:3], v[220:223], v[240:243], v[0:3]
	s_barrier
	s_add_u32 s51, s22, 0x200
	s_addc_u32 s52, s23, 0
	s_add_u32 s53, s24, 0x200
	s_addc_u32 s54, s25, 0
	s_add_u32 s6, s22, 0x160180
	s_addc_u32 s7, s23, 0
	s_mov_b32 s55, 0

.LBB0_1404:
	ds_read_b128 v[0:3], v138
	ds_read_b128 v[4:7], v138 offset:1024
	ds_read_b128 v[8:11], v138 offset:2048
	ds_read_b128 v[12:15], v138 offset:3072
	ds_read_b128 v[16:19], v139
	ds_read_b128 v[20:23], v139 offset:1024
	ds_read_b128 v[24:27], v139 offset:2048
	ds_read_b128 v[28:31], v139 offset:3072
	ds_read_b128 v[32:35], v140
	ds_read_b128 v[36:39], v140 offset:1024
	ds_read_b128 v[40:43], v140 offset:2048
	ds_read_b128 v[44:47], v140 offset:3072
	ds_read_b128 v[48:51], v140 offset:4096
	ds_read_b128 v[52:55], v140 offset:5120
	ds_read_b128 v[56:59], v140 offset:6144
	ds_read_b128 v[60:63], v140 offset:7168
	s_add_i32 s50, s50, 1
	s_mul_i32 s2, s50, s23
	s_mul_hi_u32 s4, s50, s33
	s_add_i32 s2, s4, s2
	s_mul_i32 s4, s50, s33
	s_add_u32 s4, s4, s87
	s_addc_u32 s5, s2, s48
	v_cmp_lt_i64_e64 s[6:7], s[4:5], v[128:129]
	s_mov_b64 s[18:19], -1
	s_and_b64 vcc, exec, s[6:7]
	s_cbranch_vccnz .LBB0_1406
	s_ashr_i32 s17, s16, 31
	s_mov_b64 s[18:19], 0
.LBB0_1406:
	s_andn2_b64 vcc, exec, s[18:19]
	s_cbranch_vccnz .LBB0_1408
	s_ashr_i32 s2, s4, 31
	s_lshr_b32 s2, s2, 29
	s_add_i32 s2, s4, s2
	s_ashr_i32 s5, s2, 3
	s_and_b32 s2, s2, -8
	s_sub_i32 s2, s4, s2
	s_cmp_lt_i32 s2, 0
	s_cselect_b32 s4, s46, s45
	s_mul_i32 s2, s4, s2
	s_add_i32 s2, s2, s5
	s_mul_hi_i32 s4, s2, 0x92492493
	s_add_i32 s4, s4, s2
	s_lshr_b32 s5, s4, 31
	s_ashr_i32 s4, s4, 8
	s_add_i32 s4, s4, s5
	s_lshl_b32 s5, s4, 3
	s_sub_i32 s14, s38, s5
	s_min_i32 s15, s14, 8
	s_abs_i32 s14, s15
	v_cvt_f32_u32_e32 v255, s14
	s_sub_i32 s17, 0, s14
	s_mulk_i32 s4, 0x1c0
	s_sub_i32 s2, s2, s4
	v_rcp_iflag_f32_e32 v255, v255
	s_abs_i32 s4, s2
	s_xor_b32 s16, s2, s15
	s_ashr_i32 s16, s16, 31
	v_mul_f32_e32 v255, 0x4f7ffffe, v255
	v_cvt_u32_f32_e32 v255, v255
	s_nop 0
	v_readfirstlane_b32 s18, v255
	s_mul_i32 s17, s17, s18
	s_mul_hi_u32 s17, s18, s17
	s_add_i32 s18, s18, s17
	s_mul_hi_u32 s17, s4, s18
	s_mul_i32 s18, s17, s14
	s_sub_i32 s4, s4, s18
	s_add_i32 s19, s17, 1
	s_sub_i32 s18, s4, s14
	s_cmp_ge_u32 s4, s14
	s_cselect_b32 s17, s19, s17
	s_cselect_b32 s4, s18, s4
	s_add_i32 s18, s17, 1
	s_cmp_ge_u32 s4, s14
	s_cselect_b32 s4, s18, s17
	s_xor_b32 s4, s4, s16
	s_sub_i32 s14, s4, s16
	s_mul_i32 s4, s14, s15
	s_sub_i32 s2, s2, s4
	s_add_i32 s16, s2, s5
	s_ashr_i32 s17, s16, 31
	s_lshl_b64 s[4:5], s[16:17], 2
	s_add_u32 s4, s43, s4
	s_addc_u32 s5, s44, s5
	s_load_dword s53, s[4:5], 0x0
	s_waitcnt lgkmcnt(0)
.LBB0_1408:
	v_cndmask_b32_e64 v255, 0, 1, s[6:7]
	v_cmp_ne_u32_e64 s[4:5], 1, v255
	s_andn2_b64 vcc, exec, s[6:7]
	s_mov_b64 s[18:19], s[26:27]
	s_cbranch_vccnz .LBB0_1410
	s_mul_i32 s15, s53, 0x1c00000
	s_mul_hi_i32 s2, s53, 0x1c00000
	s_add_u32 s20, s41, s15
	s_addc_u32 s2, s42, s2
	s_ashr_i32 s15, s14, 31
	s_lshl_b64 s[18:19], s[14:15], 19
	s_add_u32 s18, s20, s18
	s_addc_u32 s19, s2, s19
.LBB0_1410:
	s_lshl_b64 s[20:21], s[16:17], 19
	s_add_u32 s20, s39, s20
	s_addc_u32 s21, s40, s21
	s_and_b64 s[6:7], exec, s[6:7]
	s_cselect_b32 s2, s21, s29
	s_cselect_b32 s15, s20, s28
	s_add_u32 s6, s28, 0x100
	s_addc_u32 s7, s29, 0
	s_add_u32 s36, s26, 0x100
	s_addc_u32 s37, s27, 0
	s_add_u32 s30, s28, 0x180
	s_addc_u32 s31, s29, 0
	s_add_u32 s34, s26, 0x180
	s_addc_u32 s35, s27, 0
	s_add_u32 s54, s28, 0x40080
	s_addc_u32 s55, s29, 0
	s_add_i32 m0, s47, 0xc000
	s_nop 0
	global_load_lds_dwordx4 v134, s[54:55]
	s_nop 0
	s_add_i32 m0, s47, 0xe000
	s_nop 0
	global_load_lds_dwordx4 v136, s[54:55]
	s_waitcnt vmcnt(8) lgkmcnt(0)
	s_barrier
	v_mfma_f32_16x16x128_f8f6f4 v[64:67], v[0:7], v[32:39], 0
	v_mfma_f32_16x16x128_f8f6f4 v[68:71], v[8:15], v[32:39], 0
	v_mfma_f32_16x16x128_f8f6f4 v[76:79], v[8:15], v[40:47], 0
	v_mfma_f32_16x16x128_f8f6f4 v[72:75], v[0:7], v[40:47], 0
	v_mfma_f32_16x16x128_f8f6f4 v[80:83], v[0:7], v[48:55], 0
	v_mfma_f32_16x16x128_f8f6f4 v[88:91], v[8:15], v[48:55], 0
	v_mfma_f32_16x16x128_f8f6f4 v[104:107], v[8:15], v[56:63], 0
	v_mfma_f32_16x16x128_f8f6f4 v[92:95], v[0:7], v[56:63], 0
	v_mfma_f32_16x16x128_f8f6f4 v[108:111], v[16:23], v[32:39], 0
	v_mfma_f32_16x16x128_f8f6f4 v[124:127], v[24:31], v[32:39], 0
	v_mfma_f32_16x16x128_f8f6f4 v[166:169], v[24:31], v[40:47], 0
	v_mfma_f32_16x16x128_f8f6f4 v[162:165], v[16:23], v[40:47], 0
	v_mfma_f32_16x16x128_f8f6f4 v[170:173], v[16:23], v[48:55], 0
	v_mfma_f32_16x16x128_f8f6f4 v[174:177], v[24:31], v[48:55], 0
	v_mfma_f32_16x16x128_f8f6f4 v[182:185], v[24:31], v[56:63], 0
	v_mfma_f32_16x16x128_f8f6f4 v[178:181], v[16:23], v[56:63], 0
	s_barrier
	ds_read_b128 v[32:35], v140 offset:16384
	ds_read_b128 v[36:39], v140 offset:17408
	ds_read_b128 v[40:43], v140 offset:18432
	ds_read_b128 v[44:47], v140 offset:19456
	ds_read_b128 v[48:51], v140 offset:20480
	ds_read_b128 v[52:55], v140 offset:21504
	ds_read_b128 v[56:59], v140 offset:22528
	ds_read_b128 v[60:63], v140 offset:23552
	s_add_i32 m0, s47, 0x10000
	s_nop 0
	global_load_lds_dwordx4 v135, s[36:37]
	s_nop 0
	s_add_i32 m0, s47, 0x12000
	s_nop 0
	global_load_lds_dwordx4 v137, s[36:37]
	s_add_u32 s36, s26, 0x40100
	s_addc_u32 s37, s27, 0
	s_add_i32 m0, s47, 0x14000
	s_nop 0
	global_load_lds_dwordx4 v135, s[36:37]
	s_nop 0
	s_add_i32 m0, s47, 0x16000
	s_nop 0
	global_load_lds_dwordx4 v137, s[36:37]
	s_nop 0
	s_add_i32 m0, s47, 0
	s_nop 0
	global_load_lds_dwordx4 v134, s[6:7]
	s_nop 0
	s_add_i32 m0, s47, 0x2000
	s_nop 0
	global_load_lds_dwordx4 v136, s[6:7]
	s_waitcnt vmcnt(8) lgkmcnt(0)
	s_barrier
	v_mfma_f32_16x16x128_f8f6f4 v[186:189], v[0:7], v[32:39], 0
	v_mfma_f32_16x16x128_f8f6f4 v[190:193], v[8:15], v[32:39], 0
	v_mfma_f32_16x16x128_f8f6f4 v[198:201], v[8:15], v[40:47], 0
	v_mfma_f32_16x16x128_f8f6f4 v[194:197], v[0:7], v[40:47], 0
	v_mfma_f32_16x16x128_f8f6f4 v[202:205], v[0:7], v[48:55], 0
	v_mfma_f32_16x16x128_f8f6f4 v[206:209], v[8:15], v[48:55], 0
	v_mfma_f32_16x16x128_f8f6f4 v[214:217], v[8:15], v[56:63], 0
	v_mfma_f32_16x16x128_f8f6f4 v[210:213], v[0:7], v[56:63], 0
	v_mfma_f32_16x16x128_f8f6f4 v[218:221], v[16:23], v[32:39], 0
	v_mfma_f32_16x16x128_f8f6f4 v[222:225], v[24:31], v[32:39], 0
	v_mfma_f32_16x16x128_f8f6f4 v[230:233], v[24:31], v[40:47], 0
	v_mfma_f32_16x16x128_f8f6f4 v[226:229], v[16:23], v[40:47], 0
	v_mfma_f32_16x16x128_f8f6f4 v[234:237], v[16:23], v[48:55], 0
	v_mfma_f32_16x16x128_f8f6f4 v[238:241], v[24:31], v[48:55], 0
	v_mfma_f32_16x16x128_f8f6f4 v[246:249], v[24:31], v[56:63], 0
	v_mfma_f32_16x16x128_f8f6f4 v[242:245], v[16:23], v[56:63], 0
	s_barrier
	ds_read_b128 v[0:3], v141
	ds_read_b128 v[4:7], v141 offset:1024
	ds_read_b128 v[8:11], v141 offset:2048
	ds_read_b128 v[12:15], v141 offset:3072
	ds_read_b128 v[146:149], v142
	ds_read_b128 v[150:153], v142 offset:1024
	ds_read_b128 v[154:157], v142 offset:2048
	ds_read_b128 v[158:161], v142 offset:3072
	ds_read_b128 v[16:19], v140 offset:32768
	ds_read_b128 v[20:23], v140 offset:33792
	ds_read_b128 v[24:27], v140 offset:34816
	ds_read_b128 v[28:31], v140 offset:35840
	ds_read_b128 v[32:35], v140 offset:36864
	ds_read_b128 v[36:39], v140 offset:37888
	ds_read_b128 v[40:43], v140 offset:38912
	ds_read_b128 v[44:47], v140 offset:39936
	s_add_u32 s28, s28, 0x40100
	s_addc_u32 s29, s29, 0
	s_add_i32 m0, s47, 0x4000
	s_nop 0
	global_load_lds_dwordx4 v134, s[28:29]
	s_nop 0
	s_add_i32 m0, s47, 0x6000
	s_nop 0
	global_load_lds_dwordx4 v136, s[28:29]
	s_waitcnt vmcnt(8) lgkmcnt(0)
	s_barrier
	v_mfma_f32_16x16x128_f8f6f4 v[112:115], v[0:7], v[16:23], v[64:67]
	v_mfma_f32_16x16x128_f8f6f4 v[116:119], v[8:15], v[16:23], v[68:71]
	v_mfma_f32_16x16x128_f8f6f4 v[100:103], v[0:7], v[24:31], v[72:75]
	v_mfma_f32_16x16x128_f8f6f4 v[96:99], v[8:15], v[24:31], v[76:79]
	v_mfma_f32_16x16x128_f8f6f4 v[84:87], v[0:7], v[32:39], v[80:83]
	v_mfma_f32_16x16x128_f8f6f4 v[80:83], v[8:15], v[32:39], v[88:91]
	v_mfma_f32_16x16x128_f8f6f4 v[60:63], v[0:7], v[40:47], v[92:95]
	v_mfma_f32_16x16x128_f8f6f4 v[56:59], v[8:15], v[40:47], v[104:107]
	v_mfma_f32_16x16x128_f8f6f4 v[120:123], v[146:153], v[16:23], v[108:111]
	v_mfma_f32_16x16x128_f8f6f4 v[124:127], v[154:161], v[16:23], v[124:127]
	v_mfma_f32_16x16x128_f8f6f4 v[108:111], v[146:153], v[24:31], v[162:165]
	v_mfma_f32_16x16x128_f8f6f4 v[104:107], v[154:161], v[24:31], v[166:169]
	v_mfma_f32_16x16x128_f8f6f4 v[92:95], v[146:153], v[32:39], v[170:173]
	v_mfma_f32_16x16x128_f8f6f4 v[88:91], v[154:161], v[32:39], v[174:177]
	v_mfma_f32_16x16x128_f8f6f4 v[76:79], v[146:153], v[40:47], v[178:181]
	v_mfma_f32_16x16x128_f8f6f4 v[72:75], v[154:161], v[40:47], v[182:185]
	s_barrier
	ds_read_b128 v[24:27], v140 offset:49152
	ds_read_b128 v[28:31], v140 offset:50176
	ds_read_b128 v[162:165], v140 offset:51200
	ds_read_b128 v[166:169], v140 offset:52224
	ds_read_b128 v[170:173], v140 offset:53248
	ds_read_b128 v[174:177], v140 offset:54272
	ds_read_b128 v[178:181], v140 offset:55296
	ds_read_b128 v[182:185], v140 offset:56320
	s_add_i32 m0, s47, 0x18000
	s_nop 0
	global_load_lds_dwordx4 v135, s[34:35]
	s_nop 0
	s_add_i32 m0, s47, 0x1a000
	s_nop 0
	global_load_lds_dwordx4 v137, s[34:35]
	s_add_u32 s28, s26, 0x40180
	s_addc_u32 s29, s27, 0
	s_add_i32 m0, s47, 0x1c000
	s_nop 0
	global_load_lds_dwordx4 v135, s[28:29]
	s_nop 0
	s_add_i32 m0, s47, 0x1e000
	s_nop 0
	global_load_lds_dwordx4 v137, s[28:29]
	s_nop 0
	s_add_i32 m0, s47, 0x8000
	s_nop 0
	global_load_lds_dwordx4 v134, s[30:31]
	s_nop 0
	s_add_i32 m0, s47, 0xa000
	s_nop 0
	global_load_lds_dwordx4 v136, s[30:31]
	s_waitcnt vmcnt(8) lgkmcnt(0)
	s_barrier
	v_mfma_f32_16x16x128_f8f6f4 v[52:55], v[0:7], v[24:31], v[186:189]
	v_mfma_f32_16x16x128_f8f6f4 v[48:51], v[8:15], v[24:31], v[190:193]
	v_mfma_f32_16x16x128_f8f6f4 v[36:39], v[0:7], v[162:169], v[194:197]
	v_mfma_f32_16x16x128_f8f6f4 v[32:35], v[8:15], v[162:169], v[198:201]
	v_mfma_f32_16x16x128_f8f6f4 v[20:23], v[0:7], v[170:177], v[202:205]
	v_mfma_f32_16x16x128_f8f6f4 v[16:19], v[8:15], v[170:177], v[206:209]
	v_mfma_f32_16x16x128_f8f6f4 v[4:7], v[0:7], v[178:185], v[210:213]
	v_mfma_f32_16x16x128_f8f6f4 v[0:3], v[8:15], v[178:185], v[214:217]
	v_mfma_f32_16x16x128_f8f6f4 v[68:71], v[146:153], v[24:31], v[218:221]
	v_mfma_f32_16x16x128_f8f6f4 v[64:67], v[154:161], v[24:31], v[222:225]
	v_mfma_f32_16x16x128_f8f6f4 v[44:47], v[146:153], v[162:169], v[226:229]
	v_mfma_f32_16x16x128_f8f6f4 v[40:43], v[154:161], v[162:169], v[230:233]
	v_mfma_f32_16x16x128_f8f6f4 v[28:31], v[146:153], v[170:177], v[234:237]
	v_mfma_f32_16x16x128_f8f6f4 v[24:27], v[154:161], v[170:177], v[238:241]
	v_mfma_f32_16x16x128_f8f6f4 v[12:15], v[146:153], v[178:185], v[242:245]
	v_mfma_f32_16x16x128_f8f6f4 v[8:11], v[154:161], v[178:185], v[246:249]
	s_barrier
	s_add_u32 s17, s26, 0x200
	s_addc_u32 s54, s27, 0
	s_mov_b32 s55, 0

.LBB0_1481:
	ds_read_b128 v[0:3], v153
	ds_read_b128 v[4:7], v153 offset:1024
	ds_read_b128 v[8:11], v153 offset:2048
	ds_read_b128 v[12:15], v153 offset:3072
	ds_read_b128 v[16:19], v154
	ds_read_b128 v[20:23], v154 offset:1024
	ds_read_b128 v[24:27], v154 offset:2048
	ds_read_b128 v[28:31], v154 offset:3072
	ds_read_b128 v[32:35], v155
	ds_read_b128 v[36:39], v155 offset:1024
	ds_read_b128 v[40:43], v155 offset:2048
	ds_read_b128 v[44:47], v155 offset:3072
	ds_read_b128 v[48:51], v155 offset:4096
	ds_read_b128 v[52:55], v155 offset:5120
	ds_read_b128 v[56:59], v155 offset:6144
	ds_read_b128 v[60:63], v155 offset:7168
	s_add_i32 s45, s45, 1
	s_mul_i32 s4, s45, s46
	s_mul_hi_u32 s5, s45, s33
	s_add_i32 s5, s5, s4
	s_mul_i32 s4, s45, s33
	s_add_u32 s4, s4, s87
	s_addc_u32 s5, s5, s47
	v_cmp_ge_i64_e32 vcc, s[4:5], v[128:129]
	v_cmp_lt_i64_e64 s[6:7], s[4:5], v[128:129]
	s_cbranch_vccnz .LBB0_1483
	s_ashr_i32 s5, s4, 31
	s_lshr_b32 s5, s5, 29
	s_add_i32 s5, s4, s5
	s_ashr_i32 s18, s5, 3
	s_and_b32 s5, s5, -8
	s_sub_i32 s4, s4, s5
	s_lshr_b32 s5, s4, 31
	s_add_i32 s5, s3, s5
	s_mul_i32 s4, s5, s4
	s_add_i32 s4, s4, s18
	s_ashr_i32 s5, s4, 31
	s_lshr_b32 s5, s5, 26
	s_add_i32 s5, s4, s5
	s_ashr_i32 s18, s5, 6
	s_lshl_b32 s18, s18, 3
	s_sub_i32 s19, s3, s18
	s_min_i32 s19, s19, 8
	s_abs_i32 s20, s19
	v_cvt_f32_u32_e32 v255, s20
	s_sub_i32 s23, 0, s20
	s_andn2_b32 s5, s5, 63
	s_sub_i32 s4, s4, s5
	v_rcp_iflag_f32_e32 v255, v255
	s_abs_i32 s5, s4
	s_xor_b32 s21, s4, s19
	s_ashr_i32 s21, s21, 31
	v_mul_f32_e32 v255, 0x4f7ffffe, v255
	v_cvt_u32_f32_e32 v255, v255
	s_nop 0
	v_readfirstlane_b32 s26, v255
	s_mul_i32 s23, s23, s26
	s_mul_hi_u32 s23, s26, s23
	s_add_i32 s26, s26, s23
	s_mul_hi_u32 s23, s5, s26
	s_mul_i32 s26, s23, s20
	s_sub_i32 s5, s5, s26
	s_add_i32 s27, s23, 1
	s_sub_i32 s26, s5, s20
	s_cmp_ge_u32 s5, s20
	s_cselect_b32 s23, s27, s23
	s_cselect_b32 s5, s26, s5
	s_add_i32 s26, s23, 1
	s_cmp_ge_u32 s5, s20
	s_cselect_b32 s5, s26, s23
	s_xor_b32 s5, s5, s21
	s_sub_i32 s50, s5, s21
	s_mul_i32 s5, s50, s19
	s_sub_i32 s4, s4, s5
	s_add_i32 s18, s4, s18
	s_ashr_i32 s19, s18, 31
	s_lshl_b64 s[4:5], s[18:19], 2
	s_add_u32 s4, s38, s4
	s_addc_u32 s5, s39, s5
	s_load_dword s19, s[4:5], 0x0
	s_waitcnt lgkmcnt(0)
.LBB0_1483:
	s_nop 0
	v_cndmask_b32_e64 v255, 0, 1, s[6:7]
	v_cmp_ne_u32_e64 s[4:5], 1, v255
	s_andn2_b64 vcc, exec, s[6:7]
	s_mov_b64 s[6:7], s[28:29]
	s_cbranch_vccnz .LBB0_1485
	s_mul_i32 s6, s18, 0x1c0000
	s_mul_hi_i32 s7, s18, 0x1c0000
	s_add_u32 s6, s40, s6
	s_addc_u32 s7, s41, s7

.LBB0_1487:
	s_add_u32 s26, s28, 0x100
	s_addc_u32 s27, s29, 0
	s_add_u32 s36, s24, 0x100
	s_addc_u32 s37, s25, 0
	s_add_u32 s30, s28, 0x180
	s_addc_u32 s31, s29, 0
	s_add_u32 s34, s24, 0x180
	s_addc_u32 s35, s25, 0
	s_add_u32 s52, s28, 0xe0080
	s_addc_u32 s53, s29, 0
	s_add_i32 m0, s44, 0xc000
	s_nop 0
	global_load_lds_dwordx4 v149, s[52:53]
	s_nop 0
	s_add_i32 m0, s44, 0xe000
	s_nop 0
	global_load_lds_dwordx4 v151, s[52:53]
	s_waitcnt vmcnt(8) lgkmcnt(0)
	s_barrier
	v_mfma_f32_16x16x128_f8f6f4 v[64:67], v[0:7], v[32:39], 0
	v_mfma_f32_16x16x128_f8f6f4 v[68:71], v[8:15], v[32:39], 0
	v_mfma_f32_16x16x128_f8f6f4 v[76:79], v[8:15], v[40:47], 0
	v_mfma_f32_16x16x128_f8f6f4 v[72:75], v[0:7], v[40:47], 0
	v_mfma_f32_16x16x128_f8f6f4 v[80:83], v[0:7], v[48:55], 0
	v_mfma_f32_16x16x128_f8f6f4 v[88:91], v[8:15], v[48:55], 0
	v_mfma_f32_16x16x128_f8f6f4 v[104:107], v[8:15], v[56:63], 0
	v_mfma_f32_16x16x128_f8f6f4 v[92:95], v[0:7], v[56:63], 0
	v_mfma_f32_16x16x128_f8f6f4 v[108:111], v[16:23], v[32:39], 0
	v_mfma_f32_16x16x128_f8f6f4 v[124:127], v[24:31], v[32:39], 0
	v_mfma_f32_16x16x128_f8f6f4 v[162:165], v[24:31], v[40:47], 0
	v_mfma_f32_16x16x128_f8f6f4 v[158:161], v[16:23], v[40:47], 0
	v_mfma_f32_16x16x128_f8f6f4 v[166:169], v[16:23], v[48:55], 0
	v_mfma_f32_16x16x128_f8f6f4 v[170:173], v[24:31], v[48:55], 0
	v_mfma_f32_16x16x128_f8f6f4 v[178:181], v[24:31], v[56:63], 0
	v_mfma_f32_16x16x128_f8f6f4 v[174:177], v[16:23], v[56:63], 0
	s_barrier
	ds_read_b128 v[32:35], v155 offset:16384
	ds_read_b128 v[36:39], v155 offset:17408
	ds_read_b128 v[40:43], v155 offset:18432
	ds_read_b128 v[44:47], v155 offset:19456
	ds_read_b128 v[48:51], v155 offset:20480
	ds_read_b128 v[52:55], v155 offset:21504
	ds_read_b128 v[56:59], v155 offset:22528
	ds_read_b128 v[60:63], v155 offset:23552
	s_add_i32 m0, s44, 0x10000
	s_nop 0
	global_load_lds_dwordx4 v150, s[36:37]
	s_nop 0
	s_add_i32 m0, s44, 0x12000
	s_nop 0
	global_load_lds_dwordx4 v152, s[36:37]
	s_add_u32 s36, s24, 0xe0100
	s_addc_u32 s37, s25, 0
	s_add_i32 m0, s44, 0x14000
	s_nop 0
	global_load_lds_dwordx4 v150, s[36:37]
	s_nop 0
	s_add_i32 m0, s44, 0x16000
	s_nop 0
	global_load_lds_dwordx4 v152, s[36:37]
	s_nop 0
	s_add_i32 m0, s44, 0
	s_nop 0
	global_load_lds_dwordx4 v149, s[26:27]
	s_nop 0
	s_add_i32 m0, s44, 0x2000
	s_nop 0
	global_load_lds_dwordx4 v151, s[26:27]
	s_waitcnt vmcnt(8) lgkmcnt(0)
	s_barrier
	v_mfma_f32_16x16x128_f8f6f4 v[190:193], v[0:7], v[32:39], 0
	v_mfma_f32_16x16x128_f8f6f4 v[194:197], v[8:15], v[32:39], 0
	v_mfma_f32_16x16x128_f8f6f4 v[202:205], v[8:15], v[40:47], 0
	v_mfma_f32_16x16x128_f8f6f4 v[198:201], v[0:7], v[40:47], 0
	v_mfma_f32_16x16x128_f8f6f4 v[206:209], v[0:7], v[48:55], 0
	v_mfma_f32_16x16x128_f8f6f4 v[210:213], v[8:15], v[48:55], 0
	v_mfma_f32_16x16x128_f8f6f4 v[218:221], v[8:15], v[56:63], 0
	v_mfma_f32_16x16x128_f8f6f4 v[214:217], v[0:7], v[56:63], 0
	v_mfma_f32_16x16x128_f8f6f4 v[222:225], v[16:23], v[32:39], 0
	v_mfma_f32_16x16x128_f8f6f4 v[226:229], v[24:31], v[32:39], 0
	v_mfma_f32_16x16x128_f8f6f4 v[234:237], v[24:31], v[40:47], 0
	v_mfma_f32_16x16x128_f8f6f4 v[230:233], v[16:23], v[40:47], 0
	v_mfma_f32_16x16x128_f8f6f4 v[238:241], v[16:23], v[48:55], 0
	v_mfma_f32_16x16x128_f8f6f4 v[242:245], v[24:31], v[48:55], 0
	v_mfma_f32_16x16x128_f8f6f4 v[250:253], v[24:31], v[56:63], 0
	v_mfma_f32_16x16x128_f8f6f4 v[246:249], v[16:23], v[56:63], 0
	s_barrier
	ds_read_b128 v[0:3], v156
	ds_read_b128 v[4:7], v156 offset:1024
	ds_read_b128 v[16:19], v156 offset:2048
	ds_read_b128 v[20:23], v156 offset:3072
	ds_read_b128 v[132:135], v157
	ds_read_b128 v[136:139], v157 offset:1024
	ds_read_b128 v[140:143], v157 offset:2048
	ds_read_b128 v[144:147], v157 offset:3072
	ds_read_b128 v[8:11], v155 offset:32768
	ds_read_b128 v[12:15], v155 offset:33792
	ds_read_b128 v[24:27], v155 offset:34816
	ds_read_b128 v[28:31], v155 offset:35840
	ds_read_b128 v[32:35], v155 offset:36864
	ds_read_b128 v[36:39], v155 offset:37888
	ds_read_b128 v[40:43], v155 offset:38912
	ds_read_b128 v[44:47], v155 offset:39936
	s_add_u32 s28, s28, 0xe0100
	s_addc_u32 s29, s29, 0
	s_add_i32 m0, s44, 0x4000
	s_nop 0
	global_load_lds_dwordx4 v149, s[28:29]
	s_nop 0
	s_add_i32 m0, s44, 0x6000
	s_nop 0
	global_load_lds_dwordx4 v151, s[28:29]
	s_waitcnt vmcnt(8) lgkmcnt(0)
	s_barrier
	v_mfma_f32_16x16x128_f8f6f4 v[112:115], v[0:7], v[8:15], v[64:67]
	v_mfma_f32_16x16x128_f8f6f4 v[116:119], v[16:23], v[8:15], v[68:71]
	v_mfma_f32_16x16x128_f8f6f4 v[100:103], v[0:7], v[24:31], v[72:75]
	v_mfma_f32_16x16x128_f8f6f4 v[96:99], v[16:23], v[24:31], v[76:79]
	v_mfma_f32_16x16x128_f8f6f4 v[84:87], v[0:7], v[32:39], v[80:83]
	v_mfma_f32_16x16x128_f8f6f4 v[80:83], v[16:23], v[32:39], v[88:91]
	v_mfma_f32_16x16x128_f8f6f4 v[60:63], v[0:7], v[40:47], v[92:95]
	v_mfma_f32_16x16x128_f8f6f4 v[52:55], v[16:23], v[40:47], v[104:107]
	v_mfma_f32_16x16x128_f8f6f4 v[120:123], v[132:139], v[8:15], v[108:111]
	v_mfma_f32_16x16x128_f8f6f4 v[124:127], v[140:147], v[8:15], v[124:127]
	v_mfma_f32_16x16x128_f8f6f4 v[108:111], v[132:139], v[24:31], v[158:161]
	v_mfma_f32_16x16x128_f8f6f4 v[104:107], v[140:147], v[24:31], v[162:165]
	v_mfma_f32_16x16x128_f8f6f4 v[92:95], v[132:139], v[32:39], v[166:169]
	v_mfma_f32_16x16x128_f8f6f4 v[88:91], v[140:147], v[32:39], v[170:173]
	v_mfma_f32_16x16x128_f8f6f4 v[56:59], v[132:139], v[40:47], v[174:177]
	v_mfma_f32_16x16x128_f8f6f4 v[48:51], v[140:147], v[40:47], v[178:181]
	s_barrier
	ds_read_b128 v[158:161], v155 offset:49152
	ds_read_b128 v[162:165], v155 offset:50176
	ds_read_b128 v[166:169], v155 offset:51200
	ds_read_b128 v[170:173], v155 offset:52224
	ds_read_b128 v[174:177], v155 offset:53248
	ds_read_b128 v[178:181], v155 offset:54272
	ds_read_b128 v[182:185], v155 offset:55296
	ds_read_b128 v[186:189], v155 offset:56320
	s_add_i32 m0, s44, 0x18000
	s_nop 0
	global_load_lds_dwordx4 v150, s[34:35]
	s_nop 0
	s_add_i32 m0, s44, 0x1a000
	s_nop 0
	global_load_lds_dwordx4 v152, s[34:35]
	s_add_u32 s28, s24, 0xe0180
	s_addc_u32 s29, s25, 0
	s_add_i32 m0, s44, 0x1c000
	s_nop 0
	global_load_lds_dwordx4 v150, s[28:29]
	s_nop 0
	s_add_i32 m0, s44, 0x1e000
	s_nop 0
	global_load_lds_dwordx4 v152, s[28:29]
	s_nop 0
	s_add_i32 m0, s44, 0x8000
	s_nop 0
	global_load_lds_dwordx4 v149, s[30:31]
	s_nop 0
	s_add_i32 m0, s44, 0xa000
	s_nop 0
	global_load_lds_dwordx4 v151, s[30:31]
	s_waitcnt vmcnt(8) lgkmcnt(0)
	s_barrier
	v_mfma_f32_16x16x128_f8f6f4 v[68:71], v[0:7], v[158:165], v[190:193]
	v_mfma_f32_16x16x128_f8f6f4 v[64:67], v[16:23], v[158:165], v[194:197]
	v_mfma_f32_16x16x128_f8f6f4 v[36:39], v[16:23], v[166:173], v[202:205]
	v_mfma_f32_16x16x128_f8f6f4 v[44:47], v[0:7], v[166:173], v[198:201]
	v_mfma_f32_16x16x128_f8f6f4 v[28:31], v[0:7], v[174:181], v[206:209]
	v_mfma_f32_16x16x128_f8f6f4 v[24:27], v[16:23], v[174:181], v[210:213]
	v_mfma_f32_16x16x128_f8f6f4 v[8:11], v[16:23], v[182:189], v[218:221]
	v_mfma_f32_16x16x128_f8f6f4 v[12:15], v[0:7], v[182:189], v[214:217]
	v_mfma_f32_16x16x128_f8f6f4 v[76:79], v[132:139], v[158:165], v[222:225]
	v_mfma_f32_16x16x128_f8f6f4 v[72:75], v[140:147], v[158:165], v[226:229]
	v_mfma_f32_16x16x128_f8f6f4 v[32:35], v[140:147], v[166:173], v[234:237]
	v_mfma_f32_16x16x128_f8f6f4 v[40:43], v[132:139], v[166:173], v[230:233]
	v_mfma_f32_16x16x128_f8f6f4 v[20:23], v[132:139], v[174:181], v[238:241]
	v_mfma_f32_16x16x128_f8f6f4 v[16:19], v[140:147], v[174:181], v[242:245]
	v_mfma_f32_16x16x128_f8f6f4 v[0:3], v[140:147], v[182:189], v[250:253]
	v_mfma_f32_16x16x128_f8f6f4 v[4:7], v[132:139], v[182:189], v[246:249]
	s_barrier
	s_add_u32 s23, s24, 0x200
	s_addc_u32 s51, s25, 0
	s_mov_b32 s52, 0
